# speedup vs baseline: 1.0812x; 1.0135x over previous
.LBB2_58:
	v_mov_b32_e32 v187, 0x4138aa3b
	v_lshrrev_b32_e32 v38, 3, v115
	v_lshlrev_b32_e32 v40, 5, v0
	v_lshrrev_b32_e32 v107, 4, v110
	s_lshl_b32 s6, s38, 13
	v_and_or_b32 v38, v175, 2, v38
	v_and_b32_e32 v40, 0x180, v40
	v_lshlrev_b32_e32 v41, 3, v0
	s_add_i32 s6, s6, 0x12000
	v_lshlrev_b32_e32 v39, 9, v107
	v_and_or_b32 v40, v41, 24, v40
	v_lshlrev_b32_e32 v38, 5, v38
	v_lshrrev_b32_e32 v37, 3, v0
	v_or3_b32 v39, v40, v39, s6
	v_xor_b32_e32 v40, 32, v38
	v_lshl_add_u32 v191, v110, 5, s39
	v_and_b32_e32 v0, 7, v0
	v_or_b32_e32 v186, v39, v38
	v_or_b32_e32 v188, v39, v40
	v_xor_b32_e32 v40, 64, v38
	v_xor_b32_e32 v38, 0x60, v38
	v_bitop3_b32 v0, v37, v0, 6 bitop3:0x6c
	v_or_b32_e32 v190, v39, v38
	v_and_b32_e32 v1, 0x380, v122
	v_lshlrev_b32_e32 v38, 4, v0
	v_add_u32_e32 v0, s33, v115
	v_or_b32_e32 v189, v39, v40
	v_lshlrev_b32_e32 v34, 2, v34
	v_mov_b32_e32 v35, 0
	v_and_b32_e32 v122, 6, v115
	v_xor_b32_e32 v122, v122, v107
	v_lshlrev_b32_e32 v122, 4, v122
	v_lshl_add_u32 v122, v115, 7, v122
	v_add_u32_e32 v122, s6, v122
	s_mov_b32 s60, 0xffff0000
	s_mov_b32 s61, 0
	s_mov_b32 s62, 0
	s_mov_b32 s63, 0xffff
	s_mov_b32 s64, 0
	s_mov_b32 s65, 0xffff0000
	v_or_b32_e32 v39, s6, v1
	v_add_u32_e32 v192, 0x15f90, v0
	v_lshlrev_b32_e32 v0, 7, v107
	v_and_b32_e32 v1, 0x78, v41
	v_lshl_add_u64 v[126:127], s[30:31], 0, v[34:35]
	v_or3_b32 v193, v1, v0, s39
	v_add_u32_e32 v0, s33, v110
	v_mov_b32_e32 v34, v116
	v_mov_b32_e32 v37, v35
	v_lshl_or_b32 v194, v110, 16, v0
	v_lshl_add_u64 v[0:1], v[34:35], 0, v[36:37]
	v_mov_b32_e32 v36, v35
	v_mov_b32_e32 v76, v35
	v_mov_b32_e32 v77, v35
	v_lshl_add_u64 v[0:1], s[34:35], 0, v[0:1]
	v_mov_b32_e32 v34, v35
	v_mov_b32_e32 v74, v35
	v_mov_b32_e32 v75, v35
	s_mov_b32 s12, 0x3c003c00
	v_mov_b64_e32 v[80:81], v[76:77]
	v_mov_b64_e32 v[84:85], v[76:77]
	v_mov_b64_e32 v[88:89], v[76:77]
	v_mov_b64_e32 v[92:93], v[76:77]
	v_mov_b64_e32 v[96:97], v[76:77]
	v_mov_b64_e32 v[100:101], v[76:77]
	v_mov_b64_e32 v[104:105], v[76:77]
	v_mov_b64_e32 v[56:57], v[36:37]
	v_mov_b64_e32 v[60:61], v[36:37]
	v_mov_b64_e32 v[64:65], v[36:37]
	v_mov_b64_e32 v[68:69], v[36:37]
	v_mov_b64_e32 v[72:73], v[36:37]
	s_or_b32 s47, s40, 0x80
	v_lshl_add_u64 v[0:1], v[0:1], 0, 64
	s_mov_b32 s49, 0
	s_mov_b64 s[30:31], -1
	s_mov_b32 s13, s12
	s_movk_i32 s48, 0x300
	v_lshl_add_u32 v118, v114, 4, v116
	v_mov_b32_e32 v119, v165
	v_mov_b32_e32 v116, 0xc3500
	v_lshlrev_b32_e32 v128, 2, v114
	v_add_u32_e32 v196, v39, v38
	v_mov_b64_e32 v[78:79], v[74:75]
	v_mov_b64_e32 v[82:83], v[74:75]
	v_mov_b64_e32 v[86:87], v[74:75]
	v_mov_b64_e32 v[90:91], v[74:75]
	v_mov_b64_e32 v[94:95], v[74:75]
	v_mov_b64_e32 v[98:99], v[74:75]
	v_mov_b64_e32 v[102:103], v[74:75]
	v_mov_b64_e32 v[54:55], v[34:35]
	v_mov_b64_e32 v[58:59], v[34:35]
	v_mov_b64_e32 v[62:63], v[34:35]
	v_mov_b64_e32 v[66:67], v[34:35]
	v_mov_b32_e32 v197, 0
	s_mov_b32 s50, 0
	v_mov_b64_e32 v[70:71], v[34:35]
	v_mov_b32_e32 v50, v35
	v_mov_b32_e32 v51, v35
	v_mov_b32_e32 v52, v35
	v_mov_b32_e32 v53, v35
	v_mov_b32_e32 v46, v35
	v_mov_b32_e32 v47, v35
	v_mov_b32_e32 v48, v35
	v_mov_b32_e32 v49, v35
	v_mov_b32_e32 v42, v35
	v_mov_b32_e32 v43, v35
	v_mov_b32_e32 v44, v35
	v_mov_b32_e32 v45, v35
	v_mov_b32_e32 v38, v35
	v_mov_b32_e32 v39, v35
	v_mov_b32_e32 v40, v35
	v_mov_b32_e32 v41, v35
	s_waitcnt vmcnt(0)
	ds_write_b128 v196, v[10:13]
	ds_write_b128 v196, v[14:17] offset:1024
	ds_write_b128 v196, v[30:33] offset:2048
	ds_write_b128 v196, v[26:29] offset:3072
	ds_write_b128 v196, v[2:5] offset:4096
	ds_write_b128 v196, v[6:9] offset:5120
	ds_write_b128 v196, v[18:21] offset:6144
	ds_write_b128 v196, v[22:25] offset:7168
	s_mul_i32 s78, s42, 0xc00
	s_add_i32 s78, s78, s40
	v_mov_b32_e32 v183, v121
	s_lshl_b32 s6, s43, 6
	s_sub_i32 s83, s44, s6
	s_lshl_b32 s6, s43, 8
	s_add_i32 s82, s78, s6
	v_add_u32_e32 v229, s82, v172
	v_add_u32_e32 v230, s82, v173
	ds_read_u16 v224, v229 offset:0
	ds_read_u16 v225, v229 offset:32
	ds_read_u16 v226, v229 offset:64
	ds_read_u16 v227, v229 offset:96
	ds_read_u16 v232, v229 offset:128
	ds_read_u16 v233, v229 offset:160
	ds_read_u16 v234, v229 offset:192
	ds_read_u16 v235, v229 offset:224
	ds_read_b32 v183, v230
	s_waitcnt lgkmcnt(0)
	s_mov_b32 s85, s83

.Lmk_p72:
	s_mov_b32 s30, s85
	s_lshl_b32 s6, s43, 6
	s_sub_i32 s83, s44, s6
	s_lshl_b32 s6, s43, 8
	s_add_i32 s82, s78, s6
	s_mov_b32 s66, s41
	s_branch .LBB2_62
.LBB2_59:
	s_add_i32 s50, s50, 1
	v_readlane_b32 s41, v111, s50
	s_nop 0
	s_mov_b32 s66, s41
	s_add_i32 s0, s41, 63
	s_ashr_i32 s1, s0, 31
	s_lshr_b32 s1, s1, 26
	s_add_i32 s0, s0, s1
	s_ashr_i32 s45, s0, 6

.LBB2_61:
.LBB2_62:
	s_cmp_eq_u32 s49, 0
	s_cselect_b64 s[54:55], -1, 0
	s_cbranch_scc1 .LBB2_93
.LBB2_64:
	v_bfe_u32 v34, v121, 16, 4
	v_cmp_gt_i32_e64 s[56:57], s66, v110
	v_lshl_add_u32 v115, v34, 1, v191
	v_lshlrev_b32_e32 v34, 2, v34
	ds_bpermute_b32 v121, v34, v197
	v_xor_b32_e32 v34, 64, v122
	ds_read_b128 v[208:211], v122
	ds_read_b128 v[212:215], v34
	ds_read_b128 v[216:219], v122 offset:2048
	ds_read_b128 v[220:223], v34 offset:2048
	ds_read_b128 v[224:227], v122 offset:4096
	ds_read_b128 v[228:231], v34 offset:4096
	ds_read_b128 v[232:235], v122 offset:6144
	ds_read_b128 v[236:239], v34 offset:6144
	ds_read_b64_tr_b16 v[130:131], v186 offset:0
	ds_read_b64_tr_b16 v[132:133], v186 offset:2048
	ds_read_b64_tr_b16 v[134:135], v188 offset:0
	ds_read_b64_tr_b16 v[136:137], v188 offset:2048
	ds_read_b64_tr_b16 v[138:139], v189 offset:0
	ds_read_b64_tr_b16 v[140:141], v189 offset:2048
	ds_read_b64_tr_b16 v[142:143], v190 offset:0
	ds_read_b64_tr_b16 v[144:145], v190 offset:2048
	s_waitcnt vmcnt(8)
.Lmk_ua_ready:
	s_waitcnt lgkmcnt(8)
	v_mfma_f32_16x16x32_f16 v[200:203], v[240:243], v[208:211], 0
	v_mfma_f32_16x16x32_f16 v[160:163], v[240:243], v[216:219], 0
	v_mfma_f32_16x16x32_f16 v[248:251], v[240:243], v[224:227], 0
	v_mfma_f32_16x16x32_f16 v[252:255], v[240:243], v[232:235], 0
	v_mfma_f32_16x16x32_f16 v[200:203], v[244:247], v[212:215], v[200:203]
	v_mfma_f32_16x16x32_f16 v[160:163], v[244:247], v[220:223], v[160:163]
	v_mfma_f32_16x16x32_f16 v[248:251], v[244:247], v[228:231], v[248:251]
	v_mfma_f32_16x16x32_f16 v[252:255], v[244:247], v[236:239], v[252:255]
	ds_read_b64_tr_b16 v[146:147], v186 offset:4096
	ds_read_b64_tr_b16 v[148:149], v186 offset:6144
	ds_read_b64_tr_b16 v[150:151], v188 offset:4096
	ds_read_b64_tr_b16 v[152:153], v188 offset:6144
	ds_read_b64_tr_b16 v[154:155], v189 offset:4096
	ds_read_b64_tr_b16 v[156:157], v189 offset:6144
	ds_read_b64_tr_b16 v[204:205], v190 offset:4096
	ds_read_b64_tr_b16 v[206:207], v190 offset:6144
	v_cndmask_b32_e64 v34, v200, v160, s[60:61]
	v_cndmask_b32_e64 v34, v34, v248, s[62:63]
	v_cndmask_b32_e64 v34, v34, v252, s[64:65]
	v_cndmask_b32_e64 v201, v195, v185, s[54:55]
	v_add_f32_e32 v202, 0x40200000, v201
	v_add_f32_e32 v34, v34, v121
	v_mul_f32_e32 v121, 0x3e4ccccd, v34
	v_max_f32_e32 v34, v34, v121
	v_cmp_gt_f32_e32 vcc, v34, v202
	s_and_b64 s[68:69], s[56:57], vcc
	s_cmp_eq_u64 s[68:69], 0
	s_cbranch_scc0 .Lmk_max
	v_add_u32_e32 v229, s82, v172
	v_add_u32_e32 v230, s82, v173
	ds_read_u16 v224, v229 offset:0
	ds_read_u16 v225, v229 offset:32
	ds_read_u16 v226, v229 offset:64
	ds_read_u16 v227, v229 offset:96
	ds_read_u16 v232, v229 offset:128
	ds_read_u16 v233, v229 offset:160
	ds_read_u16 v234, v229 offset:192
	ds_read_u16 v235, v229 offset:224
	v_mov_b32_e32 v121, v183
	ds_read_b32 v183, v230
	v_mov_b64_e32 v[208:209], s[12:13]
	v_mov_b64_e32 v[210:211], s[12:13]

.Lmk_agg_join:
	s_cmp_lt_i32 s30, 33
	s_cbranch_scc1 .Lmk_st_done
	ds_write_b128 v196, v[2:5] offset:4096
	ds_write_b128 v196, v[6:9] offset:5120
	ds_write_b128 v196, v[18:21] offset:6144
	ds_write_b128 v196, v[22:25] offset:7168
.Lmk_st_done:
	s_cmp_lt_i32 s66, 33
	s_cbranch_scc1 .LBB2_76
	v_mfma_f32_16x16x32_f16 v[54:57], v[146:149], v[160:163], v[54:57]
	v_mfma_f32_16x16x32_f16 v[58:61], v[150:153], v[160:163], v[58:61]
	v_mfma_f32_16x16x32_f16 v[62:65], v[154:157], v[160:163], v[62:65]
	v_mfma_f32_16x16x32_f16 v[66:69], v[204:207], v[160:163], v[66:69]
	v_mfma_f32_16x16x32_f16 v[70:73], v[208:211], v[160:163], v[70:73]
.LBB2_76:
	s_and_b64 vcc, exec, s[54:55]
	s_cbranch_vccz .LBB2_110
	s_cmp_gt_i32 s50, 35
	s_cbranch_scc1 .LBB2_110
	s_add_i32 s36, s50, 2
	s_mul_hi_i32 s0, s36, 0x55555556
	s_lshr_b32 s1, s0, 31
	s_add_i32 s0, s0, s1
	s_mul_i32 s0, s0, 3
	s_sub_i32 s37, s36, s0
	s_mulk_i32 s37, 0xc00
	s_add_i32 s38, s40, s37
	v_lshl_add_u32 v36, v114, 2, v129
	s_and_saveexec_b64 s[0:1], s[4:5]
	v_lshl_add_u32 v37, v110, 2, s38
	ds_write_b32 v37, v194
	s_or_b64 exec, exec, s[0:1]
	v_lshl_add_u32 v37, v36, 2, s38
	v_lshlrev_b32_e32 v36, 2, v114
	v_sub_u32_e32 v36, v169, v36
	s_waitcnt vmcnt(8)
	v_cmp_lt_i32_e32 vcc, 0, v36
	s_and_saveexec_b64 s[0:1], vcc
	ds_write_b32 v37, v164 offset:64
	s_or_b64 exec, exec, s[0:1]
	v_cmp_lt_i32_e32 vcc, 1, v36
	s_and_saveexec_b64 s[0:1], vcc
	ds_write_b32 v37, v165 offset:68
	s_or_b64 exec, exec, s[0:1]
	v_cmp_lt_i32_e32 vcc, 2, v36
	s_and_saveexec_b64 s[0:1], vcc
	ds_write_b32 v37, v166 offset:72
	s_or_b64 exec, exec, s[0:1]
	v_cmp_lt_i32_e32 vcc, 3, v36
	s_and_saveexec_b64 s[0:1], vcc
	ds_write_b32 v37, v167 offset:76
	s_or_b64 exec, exec, s[0:1]
	v_add_u32_e32 v36, v129, v114
	v_cmp_lt_i32_e32 vcc, v119, v169
	s_and_saveexec_b64 s[0:1], vcc
	s_cbranch_execz .LBB2_109
	s_add_i32 s37, s47, s37
	v_lshl_add_u32 v130, v36, 2, s37
	v_lshlrev_b32_e32 v36, 2, v120
	v_mov_b32_e32 v37, 0
	v_mad_i64_i32 v[36:37], s[36:37], s36, v116, v[36:37]
	v_lshl_add_u64 v[36:37], v[0:1], 0, v[36:37]
	s_mov_b64 s[36:37], 0
	v_mov_b32_e32 v34, v119
	s_branch .LBB2_91
.LBB2_90:
	s_or_b64 exec, exec, s[38:39]
	v_add_u32_e32 v34, 4, v34
	v_cmp_ge_i32_e32 vcc, v34, v169
	v_add_u32_e32 v130, 16, v130
	s_or_b64 s[36:37], vcc, s[36:37]
	v_lshl_add_u64 v[36:37], v[36:37], 0, 16
	s_andn2_b64 exec, exec, s[36:37]
	s_cbranch_execz .LBB2_109
.LBB2_91:
	v_add3_u32 v131, v129, v34, 16
	v_cmp_gt_i32_e32 vcc, s48, v131
	s_and_saveexec_b64 s[38:39], vcc
	s_cbranch_execz .LBB2_90
	global_load_dword v131, v[36:37], off
	s_waitcnt vmcnt(0)
	ds_write_b32 v130, v131
	s_branch .LBB2_90
.LBB2_109:
	s_or_b64 exec, exec, s[0:1]
	s_add_i32 s11, s50, 2
	s_cmp_eq_u32 s42, s11
	s_cbranch_scc1 .Lmk_reread
.LBB2_110:
.Lmk_gather:
	s_mov_b32 s30, s83
	v_lshl_or_b32 v10, v224, 7, v176
	v_lshl_or_b32 v14, v225, 7, v176
	v_lshl_or_b32 v30, v226, 7, v176
	v_lshl_or_b32 v26, v227, 7, v176
	s_cmp_lt_i32 s83, 33
	global_load_dwordx4 v[10:13], v10, s[28:29]
	global_load_dwordx4 v[14:17], v14, s[28:29]
	global_load_dwordx4 v[30:33], v30, s[28:29]
	global_load_dwordx4 v[26:29], v26, s[28:29]
	s_cbranch_scc1 .LBB2_68
	v_lshl_or_b32 v2, v232, 7, v176
	v_lshl_or_b32 v6, v233, 7, v176
	v_lshl_or_b32 v18, v234, 7, v176
	v_lshl_or_b32 v22, v235, 7, v176
	global_load_dwordx4 v[2:5], v2, s[28:29]
	global_load_dwordx4 v[6:9], v6, s[28:29]
	global_load_dwordx4 v[18:21], v18, s[28:29]
	global_load_dwordx4 v[22:25], v22, s[28:29]
.LBB2_68:
	s_add_i32 s43, s43, 1
	s_sub_i32 s83, s83, 64
	s_add_i32 s82, s82, 0x100
	s_cmp_lg_u32 s43, s46
	s_cbranch_scc1 .LBB2_72
	s_add_i32 s10, s42, 1
	s_cmp_gt_i32 s42, 36
	s_mov_b32 s46, 2.0
	s_mov_b32 s44, 0
	s_cbranch_scc1 .LBB2_71
	v_readlane_b32 s44, v111, s10
	s_add_i32 s11, s44, 63
	s_ashr_i32 s34, s11, 31
	s_lshr_b32 s34, s34, 26
	s_add_i32 s11, s11, s34
	s_ashr_i32 s46, s11, 6
.LBB2_71:
	s_mov_b32 s43, 0
	s_mov_b32 s42, s10
	s_add_i32 s78, s78, 0xc00
	s_add_i32 s11, s40, 0x2400
	s_cmp_eq_u32 s78, s11
	s_cselect_b32 s78, s40, s78
	s_mov_b32 s83, s44
	s_mov_b32 s82, s78
.LBB2_72:
.LBB2_74:
	s_add_i32 s34, s45, -1
	s_cmp_lg_u32 s49, s34
	s_cbranch_scc1 .Lmk_tail
	s_and_b64 vcc, exec, s[54:55]
	s_cbranch_vccz .Lmk_ma_ready
	s_waitcnt vmcnt(4)

.Lmk_tail:
	s_add_i32 s49, s49, 1
	s_sub_i32 s66, s66, 64
	s_cmp_lg_u32 s49, s45
	s_cbranch_scc1 .LBB2_61
	s_cmp_eq_u32 s50, 37
	s_cbranch_scc0 .LBB2_59
	s_branch .LBB2_116
.Lmk_max:
	v_cndmask_b32_e64 v161, v185, v34, s[56:57]
	v_mov_b64_e32 v[208:209], s[12:13]
	v_mov_b64_e32 v[210:211], s[12:13]
	v_max_f32_dpp v161, v161, v161 row_shr:1 row_mask:0xf bank_mask:0xf
	v_mov_b32_e32 v121, v183
	s_nop 0
	v_max_f32_dpp v161, v161, v161 row_shr:2 row_mask:0xf bank_mask:0xf
	v_add_u32_e32 v229, s82, v172
	v_add_u32_e32 v230, s82, v173
	v_max_f32_dpp v161, v161, v161 row_shr:4 row_mask:0xf bank_mask:0xf
	ds_read_u16 v224, v229 offset:0
	ds_read_u16 v225, v229 offset:32
	v_max_f32_dpp v161, v161, v161 row_shr:8 row_mask:0xf bank_mask:0xf
	ds_read_u16 v226, v229 offset:64
	ds_read_u16 v227, v229 offset:96
	v_max_f32_dpp v161, v161, v161 row_bcast:15 row_mask:0xa bank_mask:0xf
	ds_read_u16 v232, v229 offset:128
	ds_read_u16 v233, v229 offset:160
	v_max_f32_dpp v161, v161, v161 row_bcast:31 row_mask:0xc bank_mask:0xf
	ds_read_u16 v234, v229 offset:192
	ds_read_u16 v235, v229 offset:224
	v_readlane_b32 s70, v161, 63
	ds_read_b32 v183, v230
	s_and_b64 vcc, exec, s[54:55]
	s_nop 0
	v_mov_b32_e32 v161, s70
	s_cbranch_vccz .Lmk_rescale

.Lmk_rescale:
	v_sub_f32_e32 v162, v195, v161
	v_mul_f32_e32 v162, 0x3fb8aa3b, v162
	v_exp_f32_e32 v248, v162
	s_nop 0
	v_pk_mul_f32 v[56:57], v[248:249], v[56:57] op_sel_hi:[0,1]
	v_pk_mul_f32 v[54:55], v[248:249], v[54:55] op_sel_hi:[0,1]
	v_pk_mul_f32 v[60:61], v[248:249], v[60:61] op_sel_hi:[0,1]
	v_pk_mul_f32 v[58:59], v[248:249], v[58:59] op_sel_hi:[0,1]
	v_pk_mul_f32 v[64:65], v[248:249], v[64:65] op_sel_hi:[0,1]
	v_pk_mul_f32 v[62:63], v[248:249], v[62:63] op_sel_hi:[0,1]
	v_pk_mul_f32 v[68:69], v[248:249], v[68:69] op_sel_hi:[0,1]
	v_pk_mul_f32 v[66:67], v[248:249], v[66:67] op_sel_hi:[0,1]
	v_pk_mul_f32 v[72:73], v[72:73], v[248:249] op_sel_hi:[1,0]
	v_pk_mul_f32 v[70:71], v[70:71], v[248:249] op_sel_hi:[1,0]
	s_branch .Lmk_norescale

.Lmk_reread:
	v_add_u32_e32 v229, s82, v172
	v_add_u32_e32 v230, s82, v173
	ds_read_u16 v224, v229 offset:0
	ds_read_u16 v225, v229 offset:32
	ds_read_u16 v226, v229 offset:64
	ds_read_u16 v227, v229 offset:96
	ds_read_u16 v232, v229 offset:128
	ds_read_u16 v233, v229 offset:160
	ds_read_u16 v234, v229 offset:192
	ds_read_u16 v235, v229 offset:224
	ds_read_b32 v183, v230
	s_waitcnt lgkmcnt(0)
	s_branch .Lmk_gather
.LBB2_93:
	v_lshlrev_b32_e32 v36, 4, v107
	v_lshl_or_b32 v36, s50, 8, v36
	global_load_dwordx4 v[240:243], v36, s[58:59]
	global_load_dwordx4 v[244:247], v36, s[58:59] offset:64
	s_cmp_gt_i32 s50, 35
	v_mov_b32_e32 v169, 0
	s_cbranch_scc1 .LBB2_103
	v_sub_u32_e32 v169, v174, v124
	s_add_i32 s0, s50, 2
	v_mov_b32_e32 v74, 0
	v_cndmask_b32_e64 v34, 0, v169, s[2:3]
	s_mul_i32 s0, s0, 0xc3500
	v_lshl_add_u32 v36, v124, 2, v118
	v_add_u32_dpp v34, v34, v34 row_shr:1 row_mask:0xf bank_mask:0xf bound_ctrl:1
	s_add_u32 s0, s90, s0
	s_addc_u32 s1, s91, 0
	v_add_u32_dpp v34, v34, v34 row_shr:2 row_mask:0xf bank_mask:0xf bound_ctrl:1
	v_mov_b32_e32 v120, v124
	s_nop 0
	v_add_u32_dpp v34, v34, v34 row_shr:4 row_mask:0xf bank_mask:0xf bound_ctrl:1
	global_load_dwordx4 v[164:167], v36, s[0:1]
	s_nop 0
	v_add_u32_dpp v34, v34, v34 row_shr:8 row_mask:0xf bank_mask:0xf bound_ctrl:1
	s_nop 1
	v_add_u32_dpp v34, v34, v34 row_bcast:15 row_mask:0xa bank_mask:0xf
	s_nop 1
	v_mov_b32_dpp v74, v34 row_bcast:31 row_mask:0xc bank_mask:0xf
	v_sub_u32_e32 v36, v74, v169
	v_add_u32_e32 v129, v36, v34
	v_sub_u32_e32 v36, 0x2f0, v129
	v_min_i32_e32 v169, v169, v36
